# speedup vs baseline: 1.0024x; 1.0024x over previous
.Lmy_dp_hi:
	s_cmp_gt_i32 s23, 14
	s_cbranch_scc1 .Lmy_dp_top
	s_setprio 2
	s_branch .Lmy_dp_done
